# phase H top-k unit: second half-key weight fragments get their own destinations and go out with the first half's loads
# speedup vs baseline: 1.0124x; 1.0124x over previous
.LBB0_1036:
	s_or_b64 exec, exec, s[18:19]
	s_lshl_b32 s18, s26, 16
	v_readlane_b32 s19, v255, 18
	v_and_b32_e32 v10, 15, v2
	s_or_b32 s18, s18, s19
	v_readlane_b32 s19, v255, 4
	v_or_b32_e32 v0, s62, v10
	s_add_u32 s18, s19, s18
	v_readlane_b32 s19, v255, 12
	v_ashrrev_i32_e32 v1, 31, v0
	s_addc_u32 s19, s19, 0
	v_lshlrev_b64 v[0:1], 8, v[0:1]
	v_lshl_add_u64 v[0:1], s[18:19], 0, v[0:1]
	v_and_b32_e32 v104, 48, v2
	v_and_b32_e32 v20, 63, v2
	v_lshl_add_u64 v[0:1], v[0:1], 0, v[104:105]
	v_lshrrev_b32_e32 v2, 2, v2
	s_waitcnt lgkmcnt(0)
	s_barrier
	v_and_b32_e32 v11, 12, v2
	global_load_dwordx4 v[2:5], v[0:1], off
	global_load_dwordx4 v[6:9], v[0:1], off offset:64
	global_load_dwordx4 v[24:27], v[0:1], off offset:128
	global_load_dwordx4 v[28:31], v[0:1], off offset:192
	s_mov_b64 s[70:71], 0x8000
	v_lshl_add_u64 v[134:135], v[0:1], 0, s[70:71]
	global_load_dwordx4 v[136:139], v[134:135], off
	global_load_dwordx4 v[140:143], v[134:135], off offset:64
	global_load_dwordx4 v[146:149], v[134:135], off offset:128
	global_load_dwordx4 v[150:153], v[134:135], off offset:192
	v_lshl_add_u32 v23, v10, 2, v16
	v_mul_u32_u24_e32 v10, 0x210, v10
	v_add3_u32 v21, v12, v104, v10
	ds_read_b128 v[32:35], v21
	ds_read_b128 v[36:39], v21 offset:64
	s_movk_i32 s18, 0x404
	v_mad_u32_u24 v22, v11, s18, v23
	v_mov_b32_e32 v10, 0x8080
	v_add_u32_e32 v40, 0x8400, v23
	v_mad_u32_u24 v44, v11, s18, v198
	s_mov_b32 s19, 0x8000
	v_add_u32_e32 v23, 0x8600, v23
	s_waitcnt vmcnt(7) lgkmcnt(1)
	v_mfma_f32_16x16x32_bf16 v[32:35], v[32:35], v[2:5], 0
	s_waitcnt vmcnt(6) lgkmcnt(0)
	v_mfma_f32_16x16x32_bf16 v[32:35], v[36:39], v[6:9], v[32:35]
	ds_read_b128 v[36:39], v21 offset:128
	s_waitcnt vmcnt(5) lgkmcnt(0)
	v_mfma_f32_16x16x32_bf16 v[32:35], v[36:39], v[24:27], v[32:35]
	ds_read_b128 v[36:39], v21 offset:192
	s_waitcnt vmcnt(4) lgkmcnt(0)
	v_mfma_f32_16x16x32_bf16 v[32:35], v[36:39], v[28:31], v[32:35]
	s_nop 7
	ds_write_b32 v22, v32 offset:33792
	ds_write_b32 v22, v33 offset:34820
	ds_write_b32 v22, v34 offset:35848
	ds_write_b32 v22, v35 offset:36876
	ds_read_b128 v[32:35], v21 offset:8448
	ds_read_b128 v[36:39], v21 offset:8512
	s_waitcnt lgkmcnt(1)
	v_mfma_f32_16x16x32_bf16 v[32:35], v[32:35], v[2:5], 0
	s_waitcnt lgkmcnt(0)
	v_mfma_f32_16x16x32_bf16 v[32:35], v[36:39], v[6:9], v[32:35]
	ds_read_b128 v[36:39], v21 offset:8576
	s_waitcnt lgkmcnt(0)
	v_mfma_f32_16x16x32_bf16 v[32:35], v[36:39], v[24:27], v[32:35]
	ds_read_b128 v[36:39], v21 offset:8640
	s_waitcnt lgkmcnt(0)
	v_mfma_f32_16x16x32_bf16 v[32:35], v[36:39], v[28:31], v[32:35]
	s_nop 7
	ds_write_b32 v22, v32 offset:50240
	ds_write_b32 v22, v33 offset:51268
	ds_write_b32 v22, v34 offset:52296
	ds_write_b32 v22, v35 offset:53324
	ds_read_b128 v[32:35], v21 offset:16896
	ds_read_b128 v[36:39], v21 offset:16960
	s_waitcnt lgkmcnt(1)
	v_mfma_f32_16x16x32_bf16 v[32:35], v[32:35], v[2:5], 0
	s_waitcnt lgkmcnt(0)
	v_mfma_f32_16x16x32_bf16 v[32:35], v[36:39], v[6:9], v[32:35]
	ds_read_b128 v[36:39], v21 offset:17024
	s_waitcnt lgkmcnt(0)
	v_mfma_f32_16x16x32_bf16 v[32:35], v[36:39], v[24:27], v[32:35]
	ds_read_b128 v[36:39], v21 offset:17088
	s_waitcnt lgkmcnt(0)
	v_mfma_f32_16x16x32_bf16 v[32:35], v[36:39], v[28:31], v[32:35]
	v_mad_u32_u24 v36, v11, s18, v10
	v_add_u32_e32 v10, v40, v36
	s_nop 5
	ds_write_b32 v10, v32
	v_mov_b32_e32 v10, 0x8484
	v_mad_u32_u24 v37, v11, s18, v10
	v_add_u32_e32 v10, v40, v37
	ds_write_b32 v10, v33
	v_mov_b32_e32 v10, 0x8888
	v_mad_u32_u24 v38, v11, s18, v10
	v_add_u32_e32 v10, v40, v38
	ds_write_b32 v10, v34
	v_mov_b32_e32 v10, 0x8c8c
	v_mad_u32_u24 v39, v11, s18, v10
	v_add_u32_e32 v10, v40, v39
	ds_write_b32 v10, v35
	ds_read_b128 v[32:35], v21 offset:25344
	s_waitcnt lgkmcnt(0)
	v_mfma_f32_16x16x32_bf16 v[2:5], v[32:35], v[2:5], 0
	ds_read_b128 v[32:35], v21 offset:25408
	s_waitcnt lgkmcnt(0)
	v_mfma_f32_16x16x32_bf16 v[2:5], v[32:35], v[6:9], v[2:5]
	ds_read_b128 v[6:9], v21 offset:25472
	s_waitcnt lgkmcnt(0)
	v_mfma_f32_16x16x32_bf16 v[2:5], v[6:9], v[24:27], v[2:5]
	ds_read_b128 v[6:9], v21 offset:25536
	s_waitcnt lgkmcnt(0)
	v_mfma_f32_16x16x32_bf16 v[2:5], v[6:9], v[28:31], v[2:5]
	v_mov_b32_e32 v6, 0xc0c0
	v_mad_u32_u24 v41, v11, s18, v6
	v_add_u32_e32 v6, v40, v41
	s_nop 4
	ds_write_b32 v6, v2
	v_mov_b32_e32 v2, 0xc4c4
	v_mad_u32_u24 v42, v11, s18, v2
	v_add_u32_e32 v2, v40, v42
	ds_write_b32 v2, v3
	v_mov_b32_e32 v2, 0xc8c8
	v_mad_u32_u24 v43, v11, s18, v2
	v_add_u32_e32 v2, v40, v43
	ds_write_b32 v2, v4
	v_add_u32_e32 v2, v40, v44
	ds_write_b32 v2, v5
	s_nop 0
	ds_read_b128 v[28:31], v21 offset:256
	ds_read_b128 v[32:35], v21 offset:320
	s_waitcnt vmcnt(3) lgkmcnt(1)
	v_mfma_f32_16x16x32_bf16 v[28:31], v[28:31], v[136:139], 0
	s_waitcnt vmcnt(2) lgkmcnt(0)
	v_mfma_f32_16x16x32_bf16 v[28:31], v[32:35], v[140:143], v[28:31]
	ds_read_b128 v[32:35], v21 offset:384
	s_waitcnt vmcnt(1) lgkmcnt(0)
	v_mfma_f32_16x16x32_bf16 v[28:31], v[32:35], v[146:149], v[28:31]
	ds_read_b128 v[32:35], v21 offset:448
	s_waitcnt vmcnt(0) lgkmcnt(0)
	v_mfma_f32_16x16x32_bf16 v[28:31], v[32:35], v[150:153], v[28:31]
	s_nop 7
	ds_write_b32 v22, v28 offset:34304
	ds_write_b32 v22, v29 offset:35332
	ds_write_b32 v22, v30 offset:36360
	ds_write_b32 v22, v31 offset:37388
	ds_read_b128 v[28:31], v21 offset:8704
	ds_read_b128 v[32:35], v21 offset:8768
	s_waitcnt lgkmcnt(1)
	v_mfma_f32_16x16x32_bf16 v[28:31], v[28:31], v[136:139], 0
	s_waitcnt lgkmcnt(0)
	v_mfma_f32_16x16x32_bf16 v[28:31], v[32:35], v[140:143], v[28:31]
	ds_read_b128 v[32:35], v21 offset:8832
	s_waitcnt lgkmcnt(0)
	v_mfma_f32_16x16x32_bf16 v[28:31], v[32:35], v[146:149], v[28:31]
	ds_read_b128 v[32:35], v21 offset:8896
	s_waitcnt lgkmcnt(0)
	v_mfma_f32_16x16x32_bf16 v[28:31], v[32:35], v[150:153], v[28:31]
	s_nop 7
	ds_write_b32 v22, v28 offset:50752
	ds_write_b32 v22, v29 offset:51780
	ds_write_b32 v22, v30 offset:52808
	ds_write_b32 v22, v31 offset:53836
	ds_read_b128 v[28:31], v21 offset:17152
	ds_read_b128 v[32:35], v21 offset:17216
	s_waitcnt lgkmcnt(1)
	v_mfma_f32_16x16x32_bf16 v[28:31], v[28:31], v[136:139], 0
	v_add_u32_e32 v22, v23, v36
	s_waitcnt lgkmcnt(0)
	v_mfma_f32_16x16x32_bf16 v[28:31], v[32:35], v[140:143], v[28:31]
	ds_read_b128 v[32:35], v21 offset:17280
	s_waitcnt lgkmcnt(0)
	v_mfma_f32_16x16x32_bf16 v[28:31], v[32:35], v[146:149], v[28:31]
	ds_read_b128 v[32:35], v21 offset:17344
	s_waitcnt lgkmcnt(0)
	v_mfma_f32_16x16x32_bf16 v[28:31], v[32:35], v[150:153], v[28:31]
	s_nop 7
	ds_write_b32 v22, v28
	v_add_u32_e32 v22, v23, v37
	ds_write_b32 v22, v29
	v_add_u32_e32 v22, v23, v38
	ds_write_b32 v22, v30
	v_add_u32_e32 v22, v23, v39
	ds_write_b32 v22, v31
	ds_read_b128 v[28:31], v21 offset:25600
	s_waitcnt lgkmcnt(0)
	v_mfma_f32_16x16x32_bf16 v[4:7], v[28:31], v[136:139], 0
	ds_read_b128 v[28:31], v21 offset:25664
	s_waitcnt lgkmcnt(0)
	v_mfma_f32_16x16x32_bf16 v[0:3], v[28:31], v[140:143], v[4:7]
	s_nop 4
	ds_read_b128 v[4:7], v21 offset:25728
	s_waitcnt lgkmcnt(0)
	v_mfma_f32_16x16x32_bf16 v[0:3], v[4:7], v[146:149], v[0:3]
	ds_read_b128 v[4:7], v21 offset:25792
	v_mad_u32_u24 v10, v20, s18, v17
	v_readlane_b32 s18, v255, 19
	s_waitcnt lgkmcnt(0)
	v_mfma_f32_16x16x32_bf16 v[0:3], v[4:7], v[150:153], v[0:3]
	v_add_u32_e32 v4, v23, v41
	s_nop 6
	ds_write_b32 v4, v0
	v_add_u32_e32 v0, v23, v42
	ds_write_b32 v0, v1
	v_add_u32_e32 v0, v23, v43
	ds_write_b32 v0, v2
	v_add_u32_e32 v0, v23, v44
	ds_write_b32 v0, v3
	v_add_u32_e32 v0, 0x8400, v10
	s_waitcnt lgkmcnt(0)
	s_barrier
	ds_read2_b32 v[0:1], v0 offset1:1
	s_waitcnt lgkmcnt(0)
	v_not_b32_e32 v2, v0
	v_or_b32_e32 v3, 0x80000000, v0
	v_cmp_gt_i32_e32 vcc, 0, v0
	s_nop 1
	v_cndmask_b32_e32 v0, v3, v2, vcc
	v_and_b32_e32 v0, 0xffffff80, v0
	v_or_b32_e32 v6, s18, v0
	v_add_u32_e32 v0, 0x8440, v10
	ds_read2_b32 v[2:3], v0 offset1:1
	v_readlane_b32 s18, v255, 6
	s_waitcnt lgkmcnt(0)
	v_not_b32_e32 v0, v2
	v_or_b32_e32 v4, 0x80000000, v2
	v_cmp_gt_i32_e32 vcc, 0, v2
	v_or_b32_e32 v2, 0x80000000, v1
	s_nop 0
	v_cndmask_b32_e32 v0, v4, v0, vcc
	v_and_b32_e32 v0, 0xffffff80, v0
	v_or_b32_e32 v4, s18, v0
	v_not_b32_e32 v0, v1
	v_cmp_gt_i32_e32 vcc, 0, v1
	v_readlane_b32 s18, v255, 8
	v_or_b32_e32 v1, 0x80000000, v3
	v_cndmask_b32_e32 v0, v2, v0, vcc
	v_and_b32_e32 v0, 0xffffff80, v0
	v_or_b32_e32 v7, s18, v0
	v_not_b32_e32 v0, v3
	v_cmp_gt_i32_e32 vcc, 0, v3
	v_readlane_b32 s18, v255, 10
	s_nop 0
	v_cndmask_b32_e32 v0, v1, v0, vcc
	v_and_b32_e32 v0, 0xffffff80, v0
	v_or_b32_e32 v5, s18, v0
	v_add_u32_e32 v0, 0x8408, v10
	ds_read2_b32 v[0:1], v0 offset1:1
	v_readlane_b32 s18, v255, 14
	v_max_u32_e32 v49, v4, v5
	v_min_u32_e32 v4, v4, v5
	s_waitcnt lgkmcnt(0)
	v_not_b32_e32 v2, v0
	v_or_b32_e32 v3, 0x80000000, v0
	v_cmp_gt_i32_e32 vcc, 0, v0
	s_nop 1
	v_cndmask_b32_e32 v0, v3, v2, vcc
	v_and_b32_e32 v0, 0xffffff80, v0
	v_or_b32_e32 v11, s18, v0
	v_add_u32_e32 v0, 0x8448, v10
	ds_read2_b32 v[2:3], v0 offset1:1
	v_readlane_b32 s18, v255, 16
	s_waitcnt lgkmcnt(0)
	v_not_b32_e32 v0, v2
	v_or_b32_e32 v8, 0x80000000, v2
	v_cmp_gt_i32_e32 vcc, 0, v2
	v_or_b32_e32 v2, 0x80000000, v1
	s_nop 0
	v_cndmask_b32_e32 v0, v8, v0, vcc
	v_and_b32_e32 v0, 0xffffff80, v0
	v_or_b32_e32 v8, s18, v0
	v_not_b32_e32 v0, v1
	v_cmp_gt_i32_e32 vcc, 0, v1
	v_readlane_b32 s18, v255, 23
	v_or_b32_e32 v1, 0x80000000, v3
	v_cndmask_b32_e32 v0, v2, v0, vcc
	v_and_b32_e32 v0, 0xffffff80, v0
	v_or_b32_e32 v23, s18, v0
	v_not_b32_e32 v0, v3
	v_cmp_gt_i32_e32 vcc, 0, v3
	v_readlane_b32 s18, v255, 24
	s_nop 0
	v_cndmask_b32_e32 v0, v1, v0, vcc
	v_and_b32_e32 v0, 0xffffff80, v0
	v_or_b32_e32 v9, s18, v0
	v_add_u32_e32 v0, 0x8410, v10
	ds_read2_b32 v[0:1], v0 offset1:1
	v_readlane_b32 s18, v255, 25
	v_max_u32_e32 v5, v8, v9
	v_min_u32_e32 v8, v8, v9
	s_waitcnt lgkmcnt(0)
	v_not_b32_e32 v2, v0
	v_or_b32_e32 v3, 0x80000000, v0
	v_cmp_gt_i32_e32 vcc, 0, v0
	s_nop 1
	v_cndmask_b32_e32 v0, v3, v2, vcc
	v_and_b32_e32 v0, 0xffffff80, v0
	v_or_b32_e32 v24, s18, v0
	v_add_u32_e32 v0, 0x8450, v10
	ds_read2_b32 v[2:3], v0 offset1:1
	v_readlane_b32 s18, v255, 26
	s_waitcnt lgkmcnt(0)
	v_not_b32_e32 v0, v2
	v_or_b32_e32 v21, 0x80000000, v2
	v_cmp_gt_i32_e32 vcc, 0, v2
	v_or_b32_e32 v2, 0x80000000, v1
	s_nop 0
	v_cndmask_b32_e32 v0, v21, v0, vcc
	v_and_b32_e32 v0, 0xffffff80, v0
	v_or_b32_e32 v21, s18, v0
	v_not_b32_e32 v0, v1
	v_cmp_gt_i32_e32 vcc, 0, v1
	v_readlane_b32 s18, v255, 27
	v_or_b32_e32 v1, 0x80000000, v3
	v_cndmask_b32_e32 v0, v2, v0, vcc
	v_and_b32_e32 v0, 0xffffff80, v0
	v_or_b32_e32 v27, s18, v0
	v_not_b32_e32 v0, v3
	v_cmp_gt_i32_e32 vcc, 0, v3
	v_readlane_b32 s18, v255, 28
	s_nop 0
	v_cndmask_b32_e32 v0, v1, v0, vcc
	v_and_b32_e32 v0, 0xffffff80, v0
	v_or_b32_e32 v22, s18, v0
	v_add_u32_e32 v0, 0x8418, v10
	ds_read2_b32 v[0:1], v0 offset1:1
	v_readlane_b32 s18, v255, 29
	v_max_u32_e32 v9, v21, v22
	v_min_u32_e32 v21, v21, v22
	s_waitcnt lgkmcnt(0)
	v_not_b32_e32 v2, v0
	v_or_b32_e32 v3, 0x80000000, v0
	v_cmp_gt_i32_e32 vcc, 0, v0
	s_nop 1
	v_cndmask_b32_e32 v0, v3, v2, vcc
	v_and_b32_e32 v0, 0xffffff80, v0
	v_or_b32_e32 v28, s18, v0
	v_add_u32_e32 v0, 0x8458, v10
	ds_read2_b32 v[2:3], v0 offset1:1
	v_readlane_b32 s18, v255, 30
	s_waitcnt lgkmcnt(0)
	v_not_b32_e32 v0, v2
	v_or_b32_e32 v25, 0x80000000, v2
	v_cmp_gt_i32_e32 vcc, 0, v2
	v_or_b32_e32 v2, 0x80000000, v1
	s_nop 0
	v_cndmask_b32_e32 v0, v25, v0, vcc
	v_and_b32_e32 v0, 0xffffff80, v0
	v_or_b32_e32 v25, s18, v0
	v_not_b32_e32 v0, v1
	v_cmp_gt_i32_e32 vcc, 0, v1
	v_readlane_b32 s18, v255, 31
	v_or_b32_e32 v1, 0x80000000, v3
	v_cndmask_b32_e32 v0, v2, v0, vcc
	v_and_b32_e32 v0, 0xffffff80, v0
	v_or_b32_e32 v31, s18, v0
	v_not_b32_e32 v0, v3
	v_cmp_gt_i32_e32 vcc, 0, v3
	v_readlane_b32 s18, v255, 32
	s_nop 0
	v_cndmask_b32_e32 v0, v1, v0, vcc
	v_and_b32_e32 v0, 0xffffff80, v0
	v_or_b32_e32 v26, s18, v0
	v_add_u32_e32 v0, 0x8420, v10
	ds_read2_b32 v[0:1], v0 offset1:1
	v_readlane_b32 s18, v255, 22
	v_max_u32_e32 v22, v25, v26
	v_min_u32_e32 v25, v25, v26
	s_waitcnt lgkmcnt(0)
	v_not_b32_e32 v2, v0
	v_or_b32_e32 v3, 0x80000000, v0
	v_cmp_gt_i32_e32 vcc, 0, v0
	s_nop 1
	v_cndmask_b32_e32 v0, v3, v2, vcc
	v_and_b32_e32 v0, 0xffffff80, v0
	v_or_b32_e32 v32, s18, v0
	v_add_u32_e32 v0, 0x8460, v10
	ds_read2_b32 v[2:3], v0 offset1:1
	v_readlane_b32 s18, v255, 20
	s_waitcnt lgkmcnt(0)
	v_not_b32_e32 v0, v2
	v_or_b32_e32 v29, 0x80000000, v2
	v_cmp_gt_i32_e32 vcc, 0, v2
	v_or_b32_e32 v2, 0x80000000, v1
	s_nop 0
	v_cndmask_b32_e32 v0, v29, v0, vcc
	v_and_b32_e32 v0, 0xffffff80, v0
	v_or_b32_e32 v29, s18, v0
	v_not_b32_e32 v0, v1
	v_cmp_gt_i32_e32 vcc, 0, v1
	v_readlane_b32 s18, v255, 35
	v_or_b32_e32 v1, 0x80000000, v3
	v_cndmask_b32_e32 v0, v2, v0, vcc
	v_and_b32_e32 v0, 0xffffff80, v0
	v_or_b32_e32 v33, s18, v0
	v_not_b32_e32 v0, v3
	v_cmp_gt_i32_e32 vcc, 0, v3
	v_readlane_b32 s18, v255, 37
	s_nop 0
	v_cndmask_b32_e32 v0, v1, v0, vcc
	v_and_b32_e32 v0, 0xffffff80, v0
	v_or_b32_e32 v30, s18, v0
	v_add_u32_e32 v0, 0x8428, v10
	ds_read2_b32 v[0:1], v0 offset1:1
	v_readlane_b32 s18, v255, 38
	v_max_u32_e32 v26, v29, v30
	v_min_u32_e32 v29, v29, v30
	s_waitcnt lgkmcnt(0)
	v_not_b32_e32 v2, v0
	v_or_b32_e32 v3, 0x80000000, v0
	v_cmp_gt_i32_e32 vcc, 0, v0
	s_nop 1
	v_cndmask_b32_e32 v0, v3, v2, vcc
	v_add_u32_e32 v2, 0x8468, v10
	ds_read2_b32 v[2:3], v2 offset1:1
	v_and_b32_e32 v0, 0xffffff80, v0
	v_or_b32_e32 v0, s18, v0
	s_movk_i32 s18, 0x800
	s_waitcnt lgkmcnt(0)
	v_not_b32_e32 v34, v2
	v_or_b32_e32 v35, 0x80000000, v2
	v_cmp_gt_i32_e32 vcc, 0, v2
	s_nop 1
	v_cndmask_b32_e32 v2, v35, v34, vcc
	v_and_b32_e32 v2, 0xffffff80, v2
	v_or_b32_e32 v36, s49, v2
	v_not_b32_e32 v2, v1
	v_or_b32_e32 v34, 0x80000000, v1
	v_cmp_gt_i32_e32 vcc, 0, v1
	s_nop 1
	v_cndmask_b32_e32 v1, v34, v2, vcc
	v_not_b32_e32 v2, v3
	v_or_b32_e32 v34, 0x80000000, v3
	v_cmp_gt_i32_e32 vcc, 0, v3
	v_and_b32_e32 v1, 0xffffff80, v1
	v_or_b32_e32 v1, s56, v1
	v_cndmask_b32_e32 v2, v34, v2, vcc
	v_and_b32_e32 v2, 0xffffff80, v2
	v_or_b32_e32 v37, s57, v2
	v_add_u32_e32 v2, 0x8430, v10
	ds_read2_b32 v[2:3], v2 offset1:1
	v_max_u32_e32 v30, v36, v37
	v_min_u32_e32 v36, v36, v37
	s_waitcnt lgkmcnt(0)
	v_not_b32_e32 v34, v2
	v_or_b32_e32 v35, 0x80000000, v2
	v_cmp_gt_i32_e32 vcc, 0, v2
	s_nop 1
	v_cndmask_b32_e32 v2, v35, v34, vcc
	v_and_b32_e32 v2, 0xffffff80, v2
	v_or_b32_e32 v38, s60, v2
	v_add_u32_e32 v2, 0x8470, v10
	ds_read2_b32 v[34:35], v2 offset1:1
	s_waitcnt lgkmcnt(0)
	v_not_b32_e32 v2, v34
	v_or_b32_e32 v39, 0x80000000, v34
	v_cmp_gt_i32_e32 vcc, 0, v34
	v_or_b32_e32 v34, 0x80000000, v3
	s_nop 0
	v_cndmask_b32_e32 v2, v39, v2, vcc
	v_and_b32_e32 v2, 0xffffff80, v2
	v_or_b32_e32 v39, s61, v2
	v_not_b32_e32 v2, v3
	v_cmp_gt_i32_e32 vcc, 0, v3
	v_or_b32_e32 v3, 0x80000000, v35
	s_nop 0
	v_cndmask_b32_e32 v2, v34, v2, vcc
	v_and_b32_e32 v2, 0xffffff80, v2
	v_or_b32_e32 v40, s42, v2
	v_not_b32_e32 v2, v35
	v_cmp_gt_i32_e32 vcc, 0, v35
	s_nop 1
	v_cndmask_b32_e32 v2, v3, v2, vcc
	v_and_b32_e32 v2, 0xffffff80, v2
	v_or_b32_e32 v41, s63, v2
	v_add_u32_e32 v2, 0x8438, v10
	ds_read2_b32 v[2:3], v2 offset1:1
	v_add_u32_e32 v10, 0x8478, v10
	v_max_u32_e32 v37, v39, v41
	v_min_u32_e32 v39, v39, v41
	s_waitcnt lgkmcnt(0)
	v_not_b32_e32 v34, v2
	v_or_b32_e32 v35, 0x80000000, v2
	v_cmp_gt_i32_e32 vcc, 0, v2
	s_nop 1
	v_cndmask_b32_e32 v2, v35, v34, vcc
	ds_read2_b32 v[34:35], v10 offset1:1
	v_and_b32_e32 v2, 0xffffff80, v2
	v_or_b32_e32 v2, s64, v2
	s_waitcnt lgkmcnt(0)
	v_not_b32_e32 v10, v34
	v_or_b32_e32 v42, 0x80000000, v34
	v_cmp_gt_i32_e32 vcc, 0, v34
	v_not_b32_e32 v34, v3
	s_nop 0
	v_cndmask_b32_e32 v10, v42, v10, vcc
	v_or_b32_e32 v42, 0x80000000, v3
	v_cmp_gt_i32_e32 vcc, 0, v3
	v_and_b32_e32 v10, 0xffffff80, v10
	v_or_b32_e32 v10, s65, v10
	v_cndmask_b32_e32 v3, v42, v34, vcc
	v_not_b32_e32 v34, v35
	v_or_b32_e32 v42, 0x80000000, v35
	v_cmp_gt_i32_e32 vcc, 0, v35
	v_and_b32_e32 v3, 0xffffff80, v3
	v_or_b32_e32 v3, s66, v3
	v_cndmask_b32_e32 v34, v42, v34, vcc
	v_and_b32_e32 v34, 0xffffff80, v34
	v_or_b32_e32 v34, s67, v34
	v_max_u32_e32 v35, v6, v7
	v_min_u32_e32 v6, v6, v7
	v_max_u32_e32 v7, v11, v23
	v_min_u32_e32 v11, v11, v23
	v_max_u32_e32 v23, v24, v27
	v_min_u32_e32 v24, v24, v27
	v_max_u32_e32 v27, v28, v31
	v_min_u32_e32 v28, v28, v31
	v_max_u32_e32 v31, v32, v33
	v_min_u32_e32 v32, v32, v33
	v_max_u32_e32 v33, v0, v1
	v_min_u32_e32 v0, v0, v1
	v_max_u32_e32 v1, v38, v40
	v_min_u32_e32 v38, v38, v40
	v_max_u32_e32 v40, v2, v3
	v_min_u32_e32 v2, v2, v3
	v_max_u32_e32 v41, v10, v34
	v_min_u32_e32 v10, v10, v34
	v_max_u32_e32 v3, v35, v11
	v_min_u32_e32 v11, v35, v11
	v_max_u32_e32 v35, v6, v7
	v_min_u32_e32 v6, v6, v7
	v_max_u32_e32 v7, v23, v28
	v_min_u32_e32 v23, v23, v28
	v_max_u32_e32 v28, v24, v27
	v_min_u32_e32 v24, v24, v27
	v_max_u32_e32 v27, v31, v0
	v_min_u32_e32 v0, v31, v0
	v_max_u32_e32 v31, v32, v33
	v_min_u32_e32 v32, v32, v33
	v_max_u32_e32 v33, v1, v2
	v_min_u32_e32 v1, v1, v2
	v_max_u32_e32 v2, v38, v40
	v_min_u32_e32 v38, v38, v40
	v_max_u32_e32 v34, v49, v8
	v_min_u32_e32 v8, v49, v8
	v_max_u32_e32 v49, v4, v5
	v_min_u32_e32 v4, v4, v5
	v_max_u32_e32 v5, v9, v25
	v_min_u32_e32 v9, v9, v25
	v_max_u32_e32 v25, v21, v22
	v_min_u32_e32 v21, v21, v22
	v_max_u32_e32 v22, v26, v36
	v_min_u32_e32 v26, v26, v36
	v_max_u32_e32 v36, v29, v30
	v_min_u32_e32 v29, v29, v30
	v_max_u32_e32 v30, v37, v10
	v_min_u32_e32 v10, v37, v10
	v_max_u32_e32 v37, v39, v41
	v_min_u32_e32 v39, v39, v41
	v_max_u32_e32 v40, v3, v35
	v_min_u32_e32 v3, v3, v35
	v_max_u32_e32 v35, v11, v6
	v_min_u32_e32 v6, v11, v6
	v_max_u32_e32 v11, v23, v24
	v_min_u32_e32 v23, v23, v24
	v_max_u32_e32 v24, v7, v28
	v_min_u32_e32 v7, v7, v28
	v_max_u32_e32 v28, v27, v31
	v_min_u32_e32 v27, v27, v31
	v_max_u32_e32 v31, v0, v32
	v_min_u32_e32 v0, v0, v32
	v_max_u32_e32 v32, v1, v38
	v_min_u32_e32 v1, v1, v38
	v_max_u32_e32 v38, v33, v2
	v_min_u32_e32 v2, v33, v2
	v_max_u32_e32 v41, v34, v49
	v_min_u32_e32 v34, v34, v49
	v_max_u32_e32 v49, v8, v4
	v_min_u32_e32 v4, v8, v4
	v_max_u32_e32 v8, v9, v21
	v_min_u32_e32 v9, v9, v21
	v_max_u32_e32 v21, v5, v25
	v_min_u32_e32 v5, v5, v25
	v_max_u32_e32 v25, v22, v36
	v_min_u32_e32 v22, v22, v36
	v_max_u32_e32 v36, v26, v29
	v_min_u32_e32 v26, v26, v29
	v_max_u32_e32 v29, v10, v39
	v_min_u32_e32 v10, v10, v39
	v_max_u32_e32 v39, v30, v37
	v_min_u32_e32 v30, v30, v37
	v_max_u32_e32 v33, v40, v23
	v_min_u32_e32 v23, v40, v23
	v_max_u32_e32 v40, v3, v11
	v_min_u32_e32 v3, v3, v11
	v_max_u32_e32 v11, v35, v7
	v_min_u32_e32 v7, v35, v7
	v_max_u32_e32 v35, v6, v24
	v_min_u32_e32 v6, v6, v24
	v_max_u32_e32 v24, v28, v1
	v_min_u32_e32 v1, v28, v1
	v_max_u32_e32 v28, v27, v32
	v_min_u32_e32 v27, v27, v32
	v_max_u32_e32 v32, v31, v2
	v_min_u32_e32 v2, v31, v2
	v_max_u32_e32 v31, v0, v38
	v_min_u32_e32 v0, v0, v38
	v_max_u32_e32 v37, v41, v9
	v_min_u32_e32 v9, v41, v9
	v_max_u32_e32 v41, v34, v8
	v_min_u32_e32 v8, v34, v8
	v_max_u32_e32 v34, v49, v5
	v_min_u32_e32 v5, v49, v5
	v_max_u32_e32 v49, v4, v21
	v_min_u32_e32 v4, v4, v21
	v_max_u32_e32 v21, v25, v10
	v_min_u32_e32 v10, v25, v10
	v_max_u32_e32 v25, v22, v29
	v_min_u32_e32 v22, v22, v29
	v_max_u32_e32 v29, v36, v30
	v_min_u32_e32 v30, v36, v30
	v_max_u32_e32 v36, v26, v39
	v_min_u32_e32 v26, v26, v39
	v_max_u32_e32 v38, v33, v11
	v_min_u32_e32 v11, v33, v11
	v_max_u32_e32 v33, v40, v35
	v_min_u32_e32 v35, v40, v35
	v_max_u32_e32 v40, v23, v7
	v_min_u32_e32 v7, v23, v7
	v_max_u32_e32 v23, v3, v6
	v_min_u32_e32 v3, v3, v6
	v_max_u32_e32 v6, v1, v2
	v_min_u32_e32 v1, v1, v2
	v_max_u32_e32 v2, v27, v0
	v_min_u32_e32 v0, v27, v0
	v_max_u32_e32 v27, v24, v32
	v_min_u32_e32 v24, v24, v32
	v_max_u32_e32 v32, v28, v31
	v_min_u32_e32 v28, v28, v31
	v_max_u32_e32 v39, v37, v34
	v_min_u32_e32 v34, v37, v34
	v_max_u32_e32 v37, v41, v49
	v_min_u32_e32 v41, v41, v49
	v_max_u32_e32 v49, v9, v5
	v_min_u32_e32 v5, v9, v5
	v_max_u32_e32 v9, v8, v4
	v_min_u32_e32 v4, v8, v4
	v_max_u32_e32 v8, v10, v30
	v_min_u32_e32 v10, v10, v30
	v_max_u32_e32 v30, v22, v26
	v_min_u32_e32 v22, v22, v26
	v_max_u32_e32 v26, v21, v29
	v_min_u32_e32 v21, v21, v29
	v_max_u32_e32 v29, v25, v36
	v_min_u32_e32 v25, v25, v36
	v_max_u32_e32 v31, v38, v33
	v_min_u32_e32 v33, v38, v33
	v_max_u32_e32 v38, v11, v35
	v_min_u32_e32 v11, v11, v35
	v_max_u32_e32 v35, v40, v23
	v_min_u32_e32 v23, v40, v23
	v_max_u32_e32 v40, v7, v3
	v_min_u32_e32 v3, v7, v3
	v_max_u32_e32 v7, v1, v0
	v_min_u32_e32 v0, v1, v0
	v_max_u32_e32 v1, v6, v2
	v_min_u32_e32 v2, v6, v2
	v_max_u32_e32 v6, v24, v28
	v_min_u32_e32 v24, v24, v28
	v_max_u32_e32 v28, v27, v32
	v_min_u32_e32 v27, v27, v32
	v_max_u32_e32 v36, v39, v37
	v_min_u32_e32 v37, v39, v37
	v_max_u32_e32 v39, v34, v41
	v_min_u32_e32 v34, v34, v41
	v_max_u32_e32 v41, v49, v9
	v_min_u32_e32 v9, v49, v9
	v_max_u32_e32 v49, v5, v4
	v_min_u32_e32 v4, v5, v4
	v_max_u32_e32 v5, v10, v22
	v_min_u32_e32 v10, v10, v22
	v_max_u32_e32 v22, v8, v30
	v_min_u32_e32 v8, v8, v30
	v_max_u32_e32 v30, v21, v25
	v_min_u32_e32 v21, v21, v25
	v_max_u32_e32 v25, v26, v29
	v_min_u32_e32 v26, v26, v29
	v_max_u32_e32 v32, v31, v0
	v_min_u32_e32 v0, v31, v0
	v_max_u32_e32 v31, v33, v7
	v_min_u32_e32 v7, v33, v7
	v_max_u32_e32 v33, v38, v2
	v_min_u32_e32 v2, v38, v2
	v_max_u32_e32 v38, v11, v1
	v_min_u32_e32 v1, v11, v1
	v_max_u32_e32 v11, v35, v24
	v_min_u32_e32 v24, v35, v24
	v_max_u32_e32 v35, v23, v6
	v_min_u32_e32 v6, v23, v6
	v_max_u32_e32 v23, v40, v27
	v_min_u32_e32 v27, v40, v27
	v_max_u32_e32 v40, v3, v28
	v_min_u32_e32 v3, v3, v28
	v_max_u32_e32 v29, v36, v10
	v_min_u32_e32 v10, v36, v10
	v_max_u32_e32 v36, v37, v5
	v_min_u32_e32 v5, v37, v5
	v_max_u32_e32 v37, v39, v8
	v_min_u32_e32 v8, v39, v8
	v_max_u32_e32 v39, v34, v22
	v_min_u32_e32 v22, v34, v22
	v_max_u32_e32 v34, v41, v21
	v_min_u32_e32 v21, v41, v21
	v_max_u32_e32 v41, v9, v30
	v_min_u32_e32 v9, v9, v30
	v_max_u32_e32 v30, v49, v26
	v_min_u32_e32 v26, v49, v26
	v_max_u32_e32 v49, v4, v25
	v_min_u32_e32 v4, v4, v25
	v_max_u32_e32 v28, v32, v11
	v_min_u32_e32 v11, v32, v11
	v_max_u32_e32 v32, v31, v35
	v_min_u32_e32 v31, v31, v35
	v_max_u32_e32 v35, v33, v23
	v_min_u32_e32 v23, v33, v23
	v_max_u32_e32 v33, v38, v40
	v_min_u32_e32 v38, v38, v40
	v_max_u32_e32 v40, v0, v24
	v_min_u32_e32 v0, v0, v24
	v_max_u32_e32 v24, v7, v6
	v_min_u32_e32 v6, v7, v6
	v_max_u32_e32 v7, v2, v27
	v_min_u32_e32 v2, v2, v27
	v_max_u32_e32 v27, v1, v3
	v_min_u32_e32 v1, v1, v3
	v_max_u32_e32 v25, v29, v34
	v_min_u32_e32 v29, v29, v34
	v_max_u32_e32 v34, v36, v41
	v_min_u32_e32 v36, v36, v41
	v_max_u32_e32 v41, v37, v30
	v_min_u32_e32 v30, v37, v30
	v_max_u32_e32 v37, v39, v49
	v_min_u32_e32 v39, v39, v49
	v_max_u32_e32 v49, v10, v21
	v_min_u32_e32 v10, v10, v21
	v_max_u32_e32 v21, v5, v9
	v_min_u32_e32 v5, v5, v9
	v_max_u32_e32 v9, v8, v26
	v_min_u32_e32 v8, v8, v26
	v_max_u32_e32 v26, v22, v4
	v_min_u32_e32 v4, v22, v4
	v_max_u32_e32 v3, v28, v35
	v_min_u32_e32 v28, v28, v35
	v_max_u32_e32 v35, v32, v33
	v_min_u32_e32 v32, v32, v33
	v_max_u32_e32 v33, v11, v23
	v_min_u32_e32 v11, v11, v23
	v_max_u32_e32 v23, v31, v38
	v_min_u32_e32 v31, v31, v38
	v_max_u32_e32 v38, v40, v7
	v_min_u32_e32 v7, v40, v7
	v_max_u32_e32 v40, v24, v27
	v_min_u32_e32 v24, v24, v27
	v_max_u32_e32 v27, v0, v2
	v_min_u32_e32 v0, v0, v2
	v_max_u32_e32 v2, v6, v1
	v_min_u32_e32 v1, v6, v1
	v_max_u32_e32 v22, v25, v41
	v_min_u32_e32 v25, v25, v41
	v_max_u32_e32 v41, v34, v37
	v_min_u32_e32 v34, v34, v37
	v_max_u32_e32 v37, v29, v30
	v_min_u32_e32 v29, v29, v30
	v_max_u32_e32 v30, v36, v39
	v_min_u32_e32 v36, v36, v39
	v_max_u32_e32 v39, v49, v9
	v_min_u32_e32 v9, v49, v9
	v_max_u32_e32 v49, v21, v26
	v_min_u32_e32 v21, v21, v26
	v_max_u32_e32 v26, v10, v8
	v_min_u32_e32 v8, v10, v8
	v_max_u32_e32 v10, v5, v4
	v_min_u32_e32 v4, v5, v4
	v_min_u32_e32 v6, v3, v35
	v_min_u32_e32 v42, v28, v32
	v_min_u32_e32 v43, v33, v23
	v_min_u32_e32 v44, v11, v31
	v_min_u32_e32 v45, v38, v40
	v_min_u32_e32 v46, v7, v24
	v_min_u32_e32 v47, v27, v2
	v_min_u32_e32 v48, v0, v1
	v_min_u32_e32 v5, v22, v41
	v_min_u32_e32 v50, v25, v34
	v_min_u32_e32 v51, v37, v30
	v_min_u32_e32 v52, v29, v36
	v_min_u32_e32 v53, v39, v49
	v_min_u32_e32 v54, v9, v21
	v_min_u32_e32 v55, v26, v10
	v_min_u32_e32 v56, v8, v4
	v_max3_u32 v3, v3, v35, v56
	v_max3_u32 v4, v6, v8, v4
	v_max3_u32 v6, v28, v32, v55
	v_max3_u32 v8, v42, v26, v10
	v_max3_u32 v10, v33, v23, v54
	v_max3_u32 v9, v43, v9, v21
	v_max3_u32 v11, v11, v31, v53
	v_max3_u32 v21, v44, v39, v49
	v_max3_u32 v23, v38, v40, v52
	v_max3_u32 v26, v45, v29, v36
	v_max3_u32 v7, v7, v24, v51
	v_max3_u32 v24, v46, v37, v30
	v_max3_u32 v2, v27, v2, v50
	v_max3_u32 v25, v47, v25, v34
	v_max3_u32 v0, v0, v1, v5
	v_max3_u32 v1, v48, v22, v41
	v_max_u32_e32 v5, v3, v23
	v_min_u32_e32 v3, v3, v23
	v_max_u32_e32 v22, v4, v26
	v_min_u32_e32 v4, v4, v26
	v_max_u32_e32 v23, v6, v7
	v_min_u32_e32 v6, v6, v7
	v_max_u32_e32 v7, v8, v24
	v_min_u32_e32 v8, v8, v24
	v_max_u32_e32 v24, v10, v2
	v_min_u32_e32 v2, v10, v2
	v_max_u32_e32 v10, v9, v25
	v_min_u32_e32 v9, v9, v25
	v_max_u32_e32 v25, v11, v0
	v_min_u32_e32 v0, v11, v0
	v_max_u32_e32 v11, v21, v1
	v_min_u32_e32 v1, v21, v1
	v_max_u32_e32 v21, v5, v24
	v_min_u32_e32 v5, v5, v24
	v_max_u32_e32 v24, v22, v10
	v_min_u32_e32 v10, v22, v10
	v_max_u32_e32 v22, v23, v25
	v_min_u32_e32 v23, v23, v25
	v_max_u32_e32 v25, v7, v11
	v_min_u32_e32 v7, v7, v11
	v_max_u32_e32 v11, v3, v2
	v_min_u32_e32 v2, v3, v2
	v_max_u32_e32 v3, v4, v9
	v_min_u32_e32 v4, v4, v9
	v_max_u32_e32 v9, v6, v0
	v_min_u32_e32 v0, v6, v0
	v_max_u32_e32 v6, v8, v1
	v_min_u32_e32 v1, v8, v1
	v_max_u32_e32 v8, v21, v22
	v_min_u32_e32 v21, v21, v22
	v_max_u32_e32 v22, v24, v25
	v_min_u32_e32 v24, v24, v25
	v_max_u32_e32 v25, v5, v23
	v_min_u32_e32 v5, v5, v23
	v_max_u32_e32 v23, v10, v7
	v_min_u32_e32 v7, v10, v7
	v_max_u32_e32 v10, v11, v9
	v_min_u32_e32 v9, v11, v9
	v_max_u32_e32 v11, v3, v6
	v_min_u32_e32 v3, v3, v6
	v_max_u32_e32 v6, v2, v0
	v_min_u32_e32 v0, v2, v0
	v_max_u32_e32 v2, v4, v1
	v_min_u32_e32 v1, v4, v1
	v_mov_b32_e32 v43, s53
	v_max_u32_e32 v41, v0, v1
	v_min_u32_e32 v42, v0, v1
	v_bitop3_b32 v1, v20, s18, v43 bitop3:0x36
	v_max_u32_e32 v28, v8, v22
	v_min_u32_e32 v29, v8, v22
	v_lshl_add_u32 v0, v20, 2, v18
	v_lshl_add_u32 v1, v1, 2, v12
	v_max_u32_e32 v30, v21, v24
	v_min_u32_e32 v21, v21, v24
	v_max_u32_e32 v31, v25, v23
	v_min_u32_e32 v32, v25, v23
	v_max_u32_e32 v33, v5, v7
	v_min_u32_e32 v34, v5, v7
	v_max_u32_e32 v35, v10, v11
	v_min_u32_e32 v36, v10, v11
	v_max_u32_e32 v37, v9, v3
	v_min_u32_e32 v38, v9, v3
	v_max_u32_e32 v39, v6, v2
	v_min_u32_e32 v40, v6, v2
	ds_write2st64_b32 v0, v28, v29 offset1:1
	ds_write2st64_b32 v0, v30, v21 offset0:2 offset1:3
	ds_write2st64_b32 v0, v31, v32 offset0:4 offset1:5
	ds_write2st64_b32 v0, v33, v34 offset0:6 offset1:7
	ds_write2st64_b32 v0, v35, v36 offset0:8 offset1:9
	ds_write2st64_b32 v0, v37, v38 offset0:10 offset1:11
	ds_write2st64_b32 v0, v39, v40 offset0:12 offset1:13
	ds_write2st64_b32 v0, v41, v42 offset0:14 offset1:15
	s_waitcnt lgkmcnt(0)
	s_barrier
	ds_read2st64_b32 v[2:3], v1 offset1:1
	ds_read2st64_b32 v[4:5], v1 offset0:2 offset1:3
	ds_read2st64_b32 v[6:7], v1 offset0:4 offset1:5
	ds_read2st64_b32 v[8:9], v1 offset0:6 offset1:7
	ds_read2st64_b32 v[10:11], v1 offset0:8 offset1:9
	ds_read2st64_b32 v[22:23], v1 offset0:10 offset1:11
	ds_read2st64_b32 v[24:25], v1 offset0:12 offset1:13
	ds_read2st64_b32 v[26:27], v1 offset0:14 offset1:15
	s_waitcnt lgkmcnt(4)
	v_max_u32_e32 v9, v35, v9
	s_waitcnt lgkmcnt(3)
	v_max_u32_e32 v11, v33, v11
	s_waitcnt lgkmcnt(2)
	v_max_u32_e32 v23, v31, v23
	s_waitcnt lgkmcnt(1)
	v_max_u32_e32 v25, v30, v25
	s_waitcnt lgkmcnt(0)
	v_max_u32_e32 v27, v28, v27
	v_max_u32_e32 v26, v29, v26
	v_max_u32_e32 v21, v21, v24
	v_max_u32_e32 v22, v32, v22
	v_max_u32_e32 v10, v34, v10
	v_max_u32_e32 v8, v36, v8
	v_max_u32_e32 v7, v37, v7
	v_max_u32_e32 v6, v38, v6
	v_max_u32_e32 v5, v39, v5
	v_max_u32_e32 v4, v40, v4
	v_max_u32_e32 v3, v41, v3
	v_max_u32_e32 v2, v42, v2
	v_max_u32_e32 v24, v27, v9
	v_min_u32_e32 v9, v27, v9
	v_max_u32_e32 v27, v26, v8
	v_min_u32_e32 v8, v26, v8
	v_max_u32_e32 v26, v25, v7
	v_min_u32_e32 v7, v25, v7
	v_max_u32_e32 v25, v21, v6
	v_min_u32_e32 v6, v21, v6
	v_max_u32_e32 v21, v23, v5
	v_min_u32_e32 v5, v23, v5
	v_max_u32_e32 v23, v22, v4
	v_min_u32_e32 v4, v22, v4
	v_max_u32_e32 v22, v11, v3
	v_min_u32_e32 v3, v11, v3
	v_max_u32_e32 v11, v10, v2
	v_min_u32_e32 v2, v10, v2
	v_max_u32_e32 v10, v24, v21
	v_min_u32_e32 v21, v24, v21
	v_max_u32_e32 v24, v27, v23
	v_min_u32_e32 v23, v27, v23
	v_max_u32_e32 v27, v26, v22
	v_min_u32_e32 v22, v26, v22
	v_max_u32_e32 v26, v25, v11
	v_min_u32_e32 v11, v25, v11
	v_max_u32_e32 v25, v9, v5
	v_min_u32_e32 v5, v9, v5
	v_max_u32_e32 v9, v8, v4
	v_min_u32_e32 v4, v8, v4
	v_max_u32_e32 v8, v7, v3
	v_min_u32_e32 v3, v7, v3
	v_max_u32_e32 v7, v6, v2
	v_min_u32_e32 v2, v6, v2
	v_max_u32_e32 v6, v10, v27
	v_min_u32_e32 v10, v10, v27
	v_max_u32_e32 v27, v24, v26
	v_min_u32_e32 v24, v24, v26
	v_max_u32_e32 v28, v21, v22
	v_min_u32_e32 v22, v21, v22
	v_max_u32_e32 v21, v23, v11
	v_min_u32_e32 v29, v23, v11
	v_max_u32_e32 v30, v25, v8
	v_min_u32_e32 v8, v25, v8
	v_max_u32_e32 v25, v9, v7
	v_min_u32_e32 v7, v9, v7
	v_min_u32_e32 v32, v5, v3
	v_max_u32_e32 v33, v4, v2
	v_min_u32_e32 v2, v4, v2
	s_movk_i32 s18, 0x1000
	v_max_u32_e32 v31, v5, v3
	v_max_u32_e32 v26, v6, v27
	v_min_u32_e32 v5, v6, v27
	v_max_u32_e32 v11, v10, v24
	v_min_u32_e32 v3, v10, v24
	v_max_u32_e32 v23, v28, v21
	v_min_u32_e32 v6, v28, v21
	v_max_u32_e32 v21, v22, v29
	v_min_u32_e32 v4, v22, v29
	v_max_u32_e32 v22, v8, v7
	v_min_u32_e32 v7, v8, v7
	v_max_u32_e32 v24, v32, v2
	v_min_u32_e32 v8, v32, v2
	v_bitop3_b32 v2, v20, s18, v43 bitop3:0x36
	v_max_u32_e32 v27, v30, v25
	v_min_u32_e32 v9, v30, v25
	v_max_u32_e32 v25, v31, v33
	v_min_u32_e32 v10, v31, v33
	v_lshl_add_u32 v2, v2, 2, v12
	s_and_b64 vcc, exec, s[58:59]
	ds_write2st64_b32 v0, v26, v5 offset0:132 offset1:133
	ds_write2st64_b32 v0, v11, v3 offset0:134 offset1:135
	ds_write2st64_b32 v0, v23, v6 offset0:136 offset1:137
	ds_write2st64_b32 v0, v21, v4 offset0:138 offset1:139
	ds_write2st64_b32 v0, v27, v9 offset0:140 offset1:141
	ds_write2st64_b32 v0, v22, v7 offset0:142 offset1:143
	ds_write2st64_b32 v0, v25, v10 offset0:144 offset1:145
	ds_write2st64_b32 v0, v24, v8 offset0:146 offset1:147
	s_waitcnt lgkmcnt(0)
	s_barrier
	s_cbranch_vccz .LBB0_1038
	ds_read2st64_b32 v[28:29], v2 offset0:146 offset1:147
	ds_read2st64_b32 v[30:31], v2 offset0:138 offset1:139
	ds_read2st64_b32 v[32:33], v2 offset0:142 offset1:143
	ds_read2st64_b32 v[34:35], v2 offset0:144 offset1:145
	ds_read2st64_b32 v[36:37], v2 offset0:134 offset1:135
	ds_read2st64_b32 v[38:39], v2 offset0:136 offset1:137
	s_waitcnt lgkmcnt(5)
	v_max_u32_e32 v29, v26, v29
	s_waitcnt lgkmcnt(4)
	v_max_u32_e32 v31, v27, v31
	ds_read2st64_b32 v[26:27], v2 offset0:140 offset1:141
	ds_read2st64_b32 v[40:41], v2 offset0:132 offset1:133
	s_waitcnt lgkmcnt(5)
	v_max_u32_e32 v23, v23, v33
	s_waitcnt lgkmcnt(3)
	v_max_u32_e32 v25, v25, v37
	v_max_u32_e32 v11, v11, v35
	s_waitcnt lgkmcnt(2)
	v_max_u32_e32 v22, v22, v39
	s_waitcnt lgkmcnt(1)
	v_max_u32_e32 v21, v21, v27
	s_waitcnt lgkmcnt(0)
	v_max_u32_e32 v24, v24, v41
	v_max_u32_e32 v5, v5, v28
	v_max_u32_e32 v9, v9, v30
	v_max_u32_e32 v6, v6, v32
	v_max_u32_e32 v10, v10, v36
	v_max_u32_e32 v3, v3, v34
	v_max_u32_e32 v7, v7, v38
	v_max_u32_e32 v4, v4, v26
	v_max_u32_e32 v8, v8, v40
	v_min_u32_e32 v42, v29, v31
	v_min_u32_e32 v33, v23, v25
	v_min_u32_e32 v35, v11, v22
	v_min_u32_e32 v27, v21, v24
	v_min_u32_e32 v28, v5, v9
	v_min_u32_e32 v30, v6, v10
	v_min_u32_e32 v34, v3, v7
	v_min_u32_e32 v26, v4, v8
	v_min_u32_e32 v37, v42, v33
	v_min_u32_e32 v39, v35, v27
	v_min_u32_e32 v32, v28, v30
	v_min_u32_e32 v36, v34, v26
	v_max_u32_e32 v33, v42, v33
	v_max_u32_e32 v27, v35, v27
	v_max_u32_e32 v28, v28, v30
	v_max_u32_e32 v26, v34, v26
	v_min_u32_e32 v35, v33, v27
	v_min_u32_e32 v30, v28, v26
	v_max_u32_e32 v27, v33, v27
	v_max_u32_e32 v26, v28, v26
	v_min_u32_e32 v28, v27, v26
	v_max_u32_e32 v26, v27, v26
	v_max_u32_e32 v27, v29, v31
	v_max_u32_e32 v23, v23, v25
	v_max_u32_e32 v11, v11, v22
	v_max_u32_e32 v21, v21, v24
	v_max_u32_e32 v5, v5, v9
	v_max_u32_e32 v6, v6, v10
	v_max_u32_e32 v3, v3, v7
	v_max_u32_e32 v4, v4, v8
	v_min_u32_e32 v25, v27, v23
	v_min_u32_e32 v22, v11, v21
	v_min_u32_e32 v9, v5, v6
	v_min_u32_e32 v7, v3, v4
	v_min_u32_e32 v24, v25, v22
	v_min_u32_e32 v8, v9, v7
	v_max_u32_e32 v22, v25, v22
	v_max_u32_e32 v7, v9, v7
	v_min_u32_e32 v9, v22, v7
	v_max_u32_e32 v7, v22, v7
	v_max_u32_e32 v22, v27, v23
	v_max_u32_e32 v11, v11, v21
	v_max_u32_e32 v5, v5, v6
	v_max_u32_e32 v3, v3, v4
	v_min_u32_e32 v21, v22, v11
	v_min_u32_e32 v4, v5, v3
	v_max_u32_e32 v11, v22, v11
	v_max_u32_e32 v3, v5, v3
	v_min_u32_e32 v41, v37, v39
	v_min_u32_e32 v38, v32, v36
	v_max_u32_e32 v37, v37, v39
	v_max_u32_e32 v32, v32, v36
	v_min_u32_e32 v5, v11, v3
	v_max_u32_e32 v3, v11, v3
	v_lshl_add_u32 v11, v20, 2, v19
	v_min_u32_e32 v40, v41, v38
	v_max_u32_e32 v38, v41, v38
	v_min_u32_e32 v36, v37, v32
	v_max_u32_e32 v32, v37, v32
	v_min_u32_e32 v34, v35, v30
	v_max_u32_e32 v30, v35, v30
	v_min_u32_e32 v10, v24, v8
	v_max_u32_e32 v8, v24, v8
	v_min_u32_e32 v6, v21, v4
	v_max_u32_e32 v4, v21, v4
	ds_write2st64_b32 v11, v3, v5 offset1:1
	ds_write2st64_b32 v11, v4, v6 offset0:2 offset1:3
	ds_write2st64_b32 v11, v7, v9 offset0:4 offset1:5
	ds_write2st64_b32 v11, v8, v10 offset0:6 offset1:7
	ds_write2st64_b32 v11, v26, v28 offset0:8 offset1:9
	ds_write2st64_b32 v11, v30, v34 offset0:10 offset1:11
	ds_write2st64_b32 v11, v32, v36 offset0:12 offset1:13
	ds_write2st64_b32 v11, v38, v40 offset0:14 offset1:15
